# v38 + counted vmcnt(24) waits in the in-GEMM weight-conversion bursts (in-proj, FFN-up) instead of hipcc's vmcnt(0) drains before the slot-3 loads and before slot-0 processing
# speedup vs baseline: 1.0081x; 1.0081x over previous
; #define PG8_LAS __attribute__((address_space(3)))
; #define LAS __attribute__((address_space(3)))
; __device__ __forceinline__ KA ka_get() { KA p = (KA)__builtin_amdgcn_kernarg_segment_ptr(); asm volatile("" : "+s"(p)); return p; }
; #define CV_LOAD(j, R) do { ConvTile c_; if (CV_VALID(j) && CV_DEC(CV_TILE(j), c_)) conv_load(c_.W, c_.N, c_.k0, c_.n0, wave, lane, R); } while (0)
; #define CV_PROC(j, R) { ConvTile c_; if (!CV_VALID(j) || !CV_DEC(CV_TILE(j), c_)) break; if constexpr (MOE) conv_emit_moe(c_, R, T, tid, wave, lane); else conv_emit(c_, R, T, tid, wave, lane); }
; template <int NSLOT, bool MOE> __device__ __forceinline__ void conv_burst(const ConvHook& h, int bid, PG8_LAS unsigned char* T_, int tid) {
;     KA A = ka_get(); const int lane = tid & 63, wave = __builtin_amdgcn_readfirstlane(tid >> 6); LAS unsigned char* T = (LAS unsigned char*)T_;
;     const int p0 = (h.t0 >> 1) + bid, p1 = h.t1 >> 1;
;     ...
;     if constexpr (NSLOT == 4) {
;         f32x4 R0[8], R1[8], R2[8], R3[8];
;         CV_LOAD(0, R0); CV_LOAD(1, R1); CV_LOAD(2, R2);
;         for (int j = 0;; j += 4) {
;             CV_LOAD(j + 3, R3); CV_PROC(j, R0)
;             CV_LOAD(j + 4, R0); CV_PROC(j + 1, R1)
;             CV_LOAD(j + 5, R1); CV_PROC(j + 2, R2)
;             CV_LOAD(j + 6, R2); CV_PROC(j + 3, R3)
;         }
.LBB0_805:
	s_and_b32 s2, s73, 0x7ffffe00
	s_add_i32 s2, s28, s2
	s_addk_i32 s2, 0x100
	s_add_i32 s100, s2, 0x200
	s_cmp_lt_i32 s100, s60
	s_cselect_b32 s100, 1, 0
	s_cmp_lt_i32 s2, s60
	s_cselect_b64 s[68:69], -1, 0
	s_cmp_ge_i32 s2, s60
	s_cbranch_scc1 .LBB0_821
	s_lshl_b32 s12, s2, 1
	s_or_b32 s13, s12, 1
	s_cmpk_gt_i32 s13, 0x47ff
	s_waitcnt lgkmcnt(0)
	s_mov_b64 s[4:5], -1
	s_cbranch_scc0 .LBB0_809
	s_movk_i32 s24, 0x1c00
	s_mov_b64 s[4:5], 0
	s_cmpk_gt_u32 s12, 0x63ff
	s_mov_b64 s[6:7], 0
	s_cbranch_scc1 .LBB0_809
	s_add_i32 s13, s13, 0xb800
	s_bfe_u32 s6, s13, 0x90007
	s_mulk_i32 s6, 0x2493
	s_lshr_b32 s18, s6, 16
	s_load_dwordx2 s[6:7], s[14:15], 0xe0
	s_mul_i32 s19, s18, 0x380
	s_sub_i32 s13, s13, s19
	s_and_b32 s13, s13, 0xffff
	s_mul_hi_u32 s19, s18, 0x3800000
	s_mul_i32 s18, s18, 0x3800000
	s_waitcnt lgkmcnt(0)
	s_add_u32 s84, s6, s18
	s_addc_u32 s85, s7, s19
	s_lshl_b32 s6, s13, 3
	s_lshl_b32 s7, s13, 6
	s_and_b32 s6, s6, 0x1f80
	s_and_b32 s7, s7, 64
	s_or_b32 s65, s6, s7
	s_lshl_b32 s6, s13, 7
	s_and_b32 s42, s6, 0x700
	s_movk_i32 s24, 0x800
	s_mov_b64 s[6:7], -1

; #define GAS __attribute__((address_space(1)))
; #define CV_LOAD(j, R) do { ConvTile c_; if (CV_VALID(j) && CV_DEC(CV_TILE(j), c_)) conv_load(c_.W, c_.N, c_.k0, c_.n0, wave, lane, R); } while (0)
; __device__ __forceinline__ void conv_load(const float* W, int N, int k0, int n0, int wave, int lane, f32x4 (&r)[8]) {
;     const int n = n0 + 4 * lane; const bool ok = n < N;
;     const float* p = W + (size_t)(k0 + 8 * wave) * N + n;
; #pragma unroll
;     for (int i = 0; i < 8; ++i) r[i] = ok ? __builtin_nontemporal_load((const GAS f32x4*)(p + (size_t)i * N)) : (f32x4){0.f, 0.f, 0.f, 0.f};
; template <int NSLOT, bool MOE> __device__ __forceinline__ void conv_burst(const ConvHook& h, int bid, PG8_LAS unsigned char* T_, int tid) {
;     ...
;     if constexpr (NSLOT == 4) {
;         f32x4 R0[8], R1[8], R2[8], R3[8];
;         CV_LOAD(0, R0); CV_LOAD(1, R1); CV_LOAD(2, R2);
.LBB0_811:
	s_andn2_b64 vcc, exec, s[6:7]
	s_cbranch_vccnz .LBB0_821
	s_add_i32 s4, s65, s53
	s_ashr_i32 s5, s4, 31
	s_mul_i32 s5, s5, s24
	s_mul_hi_u32 s6, s4, s24
	s_add_i32 s5, s6, s5
	s_mul_i32 s4, s4, s24
	s_lshl_b64 s[4:5], s[4:5], 2
	s_cmp_lg_u32 s100, 0
	s_cbranch_scc1 .Lhw_fast_1
	s_waitcnt vmcnt(0)
	s_branch .Lhw_done_1
.Lhw_fast_1:
.Lhw_done_1:
	v_add_u32_e32 v98, s42, v153
	s_add_u32 s4, s84, s4
	s_addc_u32 s5, s85, s5
	v_ashrrev_i32_e32 v99, 31, v98
	v_cmp_gt_i32_e32 vcc, s24, v98
	v_lshl_add_u64 v[132:133], v[98:99], 2, s[4:5]
	v_mov_b32_e32 v98, 0
	v_mov_b32_e32 v102, 0
	v_mov_b32_e32 v103, 0
	v_mov_b32_e32 v104, 0
	v_mov_b32_e32 v105, 0
	v_mov_b32_e32 v106, 0
	v_mov_b32_e32 v107, 0
	v_mov_b32_e32 v108, 0
	v_mov_b32_e32 v109, 0
	s_and_saveexec_b64 s[4:5], vcc
	s_cbranch_execz .LBB0_814
	v_lshl_add_u64 v[100:101], s[24:25], 2, v[132:133]
	global_load_dwordx4 v[102:105], v[132:133], off nt
	global_load_dwordx4 v[106:109], v[100:101], off nt

; #define GAS __attribute__((address_space(1)))
; #define LAS __attribute__((address_space(3)))
; #define LDS_BARRIER() do { asm volatile("s_waitcnt lgkmcnt(0)" ::: "memory"); __builtin_amdgcn_s_barrier(); asm volatile("" ::: "memory"); } while (0)
; template <class RowMap>
; __device__ __forceinline__ void conv_store_fp8(const f32x4 (&r)[8], unsigned char* WT, int Kbytes, int k0bytes, int n0, const RowMap rm, LAS unsigned char* T, int tid, int wave, int lane) {
;     const int s = 2 * (lane & 3);
; #pragma unroll
;     for (int j = 0; j < 4; ++j) { const unsigned lo = pk4_fp8(r[0][j] * W8_SCALE, r[1][j] * W8_SCALE, r[2][j] * W8_SCALE, r[3][j] * W8_SCALE), hi = pk4_fp8(r[4][j] * W8_SCALE, r[5][j] * W8_SCALE, r[6][j] * W8_SCALE, r[7][j] * W8_SCALE);
;         *(LAS unsigned long long*)(T + (4 * lane + j) * 64 + 8 * (wave ^ s)) = (unsigned long long)lo | ((unsigned long long)hi << 32); }
;     LDS_BARRIER();
;     const int c16 = tid & 3, rr = tid >> 2;
; #pragma unroll
;     for (int q = 0; q < 2; ++q) { const int row = rr + 128 * q; const v4u v = *(const LAS v4u*)(T + row * 64 + 16 * (c16 ^ ((row >> 2) & 3)));
;         const int dr = rm(n0 + row); if (dr >= 0) *(GAS v4u*)(WT + (unsigned)((((dr >> 8) * (Kbytes >> 7) + (k0bytes >> 7)) << 15) + ((dr & 255) << 7) + (k0bytes & 127) + 16 * c16)) = v; }
;     LDS_BARRIER();
; }
.LBB0_827:
	s_andn2_b64 vcc, exec, s[6:7]
	s_mov_b64 s[6:7], -1
	s_cbranch_vccnz .LBB0_804
	s_cmp_lg_u32 s100, 0
	s_cbranch_scc1 .Lhw_fast_2
	s_waitcnt vmcnt(0)
	s_branch .Lhw_done_2
.Lhw_fast_2:
	s_waitcnt vmcnt(24)
.Lhw_done_2:
	v_mul_f32_e32 v131, 0x42800000, v2
	v_mul_f32_e32 v132, 0x42800000, v6
	v_med3_f32 v131, v131, s62, v236
	v_med3_f32 v149, v132, s62, v236
	v_mov_b32_e32 v132, v130
	v_cvt_pk_fp8_f32 v132, v131, v149
	v_mul_f32_e32 v133, 0x42800000, v10
	v_mul_f32_e32 v148, 0x42800000, v14
	v_med3_f32 v133, v133, s62, v236
	v_med3_f32 v148, v148, s62, v236
	v_cvt_pk_fp8_f32 v132, v133, v148 op_sel:[0,0,1]
	v_mul_f32_e32 v131, 0x42800000, v18
	v_mul_f32_e32 v133, 0x42800000, v22
	v_med3_f32 v131, v131, s62, v236
	v_med3_f32 v165, v133, s62, v236
	v_mov_b32_e32 v133, v130
	v_cvt_pk_fp8_f32 v133, v131, v165
	v_mul_f32_e32 v148, 0x42800000, v30
	v_mul_f32_e32 v149, 0x42800000, v26
	v_med3_f32 v148, v148, s62, v236
	v_med3_f32 v149, v149, s62, v236
	v_cvt_pk_fp8_f32 v133, v148, v149 op_sel:[0,0,1]
	v_mul_f32_e32 v131, 0x42800000, v3
	v_mul_f32_e32 v148, 0x42800000, v7
	v_med3_f32 v131, v131, s62, v236
	v_med3_f32 v166, v148, s62, v236
	v_mov_b32_e32 v148, v130
	v_cvt_pk_fp8_f32 v148, v131, v166
	v_mul_f32_e32 v149, 0x42800000, v11
	v_mul_f32_e32 v165, 0x42800000, v15
	v_med3_f32 v149, v149, s62, v236
	v_med3_f32 v165, v165, s62, v236
	v_cvt_pk_fp8_f32 v148, v149, v165 op_sel:[0,0,1]
	v_mul_f32_e32 v131, 0x42800000, v19
	v_mul_f32_e32 v149, 0x42800000, v23
	v_med3_f32 v131, v131, s62, v236
	v_med3_f32 v167, v149, s62, v236
	v_mov_b32_e32 v149, v130
	v_cvt_pk_fp8_f32 v149, v131, v167
	v_mul_f32_e32 v165, 0x42800000, v31
	v_mul_f32_e32 v166, 0x42800000, v27
	v_med3_f32 v165, v165, s62, v236
	v_med3_f32 v166, v166, s62, v236
	v_cvt_pk_fp8_f32 v149, v165, v166 op_sel:[0,0,1]
	v_mul_f32_e32 v131, 0x42800000, v4
	v_med3_f32 v131, v131, s62, v236
	s_cmp_lg_u32 s1, 0
	ds_write2_b64 v164, v[132:133], v[148:149] offset1:8
	v_mul_f32_e32 v132, 0x42800000, v8
	v_med3_f32 v149, v132, s62, v236
	v_mov_b32_e32 v132, v130
	v_cvt_pk_fp8_f32 v132, v131, v149
	v_mul_f32_e32 v133, 0x42800000, v12
	v_mul_f32_e32 v148, 0x42800000, v16
	v_med3_f32 v133, v133, s62, v236
	v_med3_f32 v148, v148, s62, v236
	v_cvt_pk_fp8_f32 v132, v133, v148 op_sel:[0,0,1]
	v_mul_f32_e32 v131, 0x42800000, v20
	v_mul_f32_e32 v133, 0x42800000, v24
	v_med3_f32 v131, v131, s62, v236
	v_med3_f32 v165, v133, s62, v236
	v_mov_b32_e32 v133, v130
	v_cvt_pk_fp8_f32 v133, v131, v165
	v_mul_f32_e32 v148, 0x42800000, v32
	v_mul_f32_e32 v149, 0x42800000, v28
	v_med3_f32 v148, v148, s62, v236
	v_med3_f32 v149, v149, s62, v236
	v_cvt_pk_fp8_f32 v133, v148, v149 op_sel:[0,0,1]
	v_mul_f32_e32 v131, 0x42800000, v5
	v_mul_f32_e32 v148, 0x42800000, v9
	v_med3_f32 v131, v131, s62, v236
	v_med3_f32 v166, v148, s62, v236
	v_mov_b32_e32 v148, v130
	v_cvt_pk_fp8_f32 v148, v131, v166
	v_mul_f32_e32 v149, 0x42800000, v13
	v_mul_f32_e32 v165, 0x42800000, v17
	v_med3_f32 v149, v149, s62, v236
	v_med3_f32 v165, v165, s62, v236
	v_cvt_pk_fp8_f32 v148, v149, v165 op_sel:[0,0,1]
	v_mul_f32_e32 v131, 0x42800000, v21
	v_mul_f32_e32 v149, 0x42800000, v25
	v_med3_f32 v131, v131, s62, v236
	v_med3_f32 v167, v149, s62, v236
	v_mov_b32_e32 v149, v130
	v_cvt_pk_fp8_f32 v149, v131, v167
	v_mul_f32_e32 v165, 0x42800000, v33
	v_mul_f32_e32 v166, 0x42800000, v29
	v_med3_f32 v165, v165, s62, v236
	v_med3_f32 v166, v166, s62, v236
	v_cvt_pk_fp8_f32 v149, v165, v166 op_sel:[0,0,1]
	v_add_u32_e32 v131, s0, v156
	ds_write2_b64 v164, v[132:133], v[148:149] offset0:16 offset1:24
	s_cbranch_scc0 .LBB0_834
	s_lshl_b32 s6, s1, 7
	v_lshlrev_b32_e32 v148, 1, v131
	s_waitcnt lgkmcnt(0)
	s_barrier
	s_add_i32 s24, s6, 0xffffff00
	v_and_b32_e32 v133, 0x7f, v131
	v_and_b32_e32 v148, 0xffffff00, v148
	s_and_b32 s7, s64, 0x7f
	v_add_u32_e32 v148, s24, v148
	v_or_b32_e32 v133, s6, v133
	s_lshr_b32 s13, s64, 7
	v_add_u32_e32 v132, s7, v158
	v_cmp_lt_i32_e32 vcc, -1, v148
	v_lshlrev_b32_e32 v133, 7, v133
	s_and_saveexec_b64 s[6:7], vcc
	s_cbranch_execz .LBB0_831
	v_add_u32_e32 v149, v157, v159
	ds_read_b128 v[166:169], v149
	v_lshrrev_b32_e32 v148, 8, v148
	v_mul_u32_u24_e32 v148, s12, v148
	v_add_lshl_u32 v148, v148, s13, 15
	v_and_b32_e32 v149, 0x7f80, v133
	v_add3_u32 v148, v149, v132, v148
	s_waitcnt lgkmcnt(0)
	global_store_dwordx4 v148, v[166:169], s[40:41]

; #define CV_LOAD(j, R) do { ConvTile c_; if (CV_VALID(j) && CV_DEC(CV_TILE(j), c_)) conv_load(c_.W, c_.N, c_.k0, c_.n0, wave, lane, R); } while (0)
; #define CV_PROC(j, R) { ConvTile c_; if (!CV_VALID(j) || !CV_DEC(CV_TILE(j), c_)) break; if constexpr (MOE) conv_emit_moe(c_, R, T, tid, wave, lane); else conv_emit(c_, R, T, tid, wave, lane); }
; template <int NSLOT, bool MOE> __device__ __forceinline__ void conv_burst(const ConvHook& h, int bid, PG8_LAS unsigned char* T_, int tid) {
;     ...
;     if constexpr (NSLOT == 4) {
;         f32x4 R0[8], R1[8], R2[8], R3[8];
;         CV_LOAD(0, R0); CV_LOAD(1, R1); CV_LOAD(2, R2);
;         for (int j = 0;; j += 4) {
;             CV_LOAD(j + 3, R3); CV_PROC(j, R0)
;             CV_LOAD(j + 4, R0); CV_PROC(j + 1, R1)
;             CV_LOAD(j + 5, R1); CV_PROC(j + 2, R2)
.LBB0_863:
	s_andn2_b64 vcc, exec, s[6:7]
	s_mov_b64 s[6:7], -1
	s_cbranch_vccnz .LBB0_804
	s_cmp_lg_u32 s100, 0
	s_cbranch_scc1 .Lhw_fast_3
	s_branch .Lhw_done_3

; #define GAS __attribute__((address_space(1)))
; #define LAS __attribute__((address_space(3)))
; #define LDS_BARRIER() do { asm volatile("s_waitcnt lgkmcnt(0)" ::: "memory"); __builtin_amdgcn_s_barrier(); asm volatile("" ::: "memory"); } while (0)
; template <class RowMap>
; __device__ __forceinline__ void conv_store_fp8(const f32x4 (&r)[8], unsigned char* WT, int Kbytes, int k0bytes, int n0, const RowMap rm, LAS unsigned char* T, int tid, int wave, int lane) {
;     const int s = 2 * (lane & 3);
; #pragma unroll
;     for (int j = 0; j < 4; ++j) { const unsigned lo = pk4_fp8(r[0][j] * W8_SCALE, r[1][j] * W8_SCALE, r[2][j] * W8_SCALE, r[3][j] * W8_SCALE), hi = pk4_fp8(r[4][j] * W8_SCALE, r[5][j] * W8_SCALE, r[6][j] * W8_SCALE, r[7][j] * W8_SCALE);
;         *(LAS unsigned long long*)(T + (4 * lane + j) * 64 + 8 * (wave ^ s)) = (unsigned long long)lo | ((unsigned long long)hi << 32); }
;     LDS_BARRIER();
;     const int c16 = tid & 3, rr = tid >> 2;
; #pragma unroll
;     for (int q = 0; q < 2; ++q) { const int row = rr + 128 * q; const v4u v = *(const LAS v4u*)(T + row * 64 + 16 * (c16 ^ ((row >> 2) & 3)));
;         const int dr = rm(n0 + row); if (dr >= 0) *(GAS v4u*)(WT + (unsigned)((((dr >> 8) * (Kbytes >> 7) + (k0bytes >> 7)) << 15) + ((dr & 255) << 7) + (k0bytes & 127) + 16 * c16)) = v; }
;     LDS_BARRIER();
; }
.Lhw_done_3:
	v_mul_f32_e32 v131, 0x42800000, v38
	v_mul_f32_e32 v132, 0x42800000, v42
	v_med3_f32 v131, v131, s62, v236
	v_med3_f32 v149, v132, s62, v236
	v_mov_b32_e32 v132, v130
	v_cvt_pk_fp8_f32 v132, v131, v149
	v_mul_f32_e32 v133, 0x42800000, v34
	v_mul_f32_e32 v148, 0x42800000, v46
	v_med3_f32 v133, v133, s62, v236
	v_med3_f32 v148, v148, s62, v236
	v_cvt_pk_fp8_f32 v132, v133, v148 op_sel:[0,0,1]
	v_mul_f32_e32 v131, 0x42800000, v50
	v_mul_f32_e32 v133, 0x42800000, v54
	v_med3_f32 v131, v131, s62, v236
	v_med3_f32 v165, v133, s62, v236
	v_mov_b32_e32 v133, v130
	v_cvt_pk_fp8_f32 v133, v131, v165
	v_mul_f32_e32 v148, 0x42800000, v62
	v_mul_f32_e32 v149, 0x42800000, v58
	v_med3_f32 v148, v148, s62, v236
	v_med3_f32 v149, v149, s62, v236
	v_cvt_pk_fp8_f32 v133, v148, v149 op_sel:[0,0,1]
	v_mul_f32_e32 v131, 0x42800000, v39
	v_mul_f32_e32 v148, 0x42800000, v43
	v_med3_f32 v131, v131, s62, v236
	v_med3_f32 v166, v148, s62, v236
	v_mov_b32_e32 v148, v130
	v_cvt_pk_fp8_f32 v148, v131, v166
	v_mul_f32_e32 v149, 0x42800000, v35
	v_mul_f32_e32 v165, 0x42800000, v47
	v_med3_f32 v149, v149, s62, v236
	v_med3_f32 v165, v165, s62, v236
	v_cvt_pk_fp8_f32 v148, v149, v165 op_sel:[0,0,1]
	v_mul_f32_e32 v131, 0x42800000, v51
	v_mul_f32_e32 v149, 0x42800000, v55
	v_med3_f32 v131, v131, s62, v236
	v_med3_f32 v167, v149, s62, v236
	v_mov_b32_e32 v149, v130
	v_cvt_pk_fp8_f32 v149, v131, v167
	v_mul_f32_e32 v165, 0x42800000, v63
	v_mul_f32_e32 v166, 0x42800000, v59
	v_med3_f32 v165, v165, s62, v236
	v_med3_f32 v166, v166, s62, v236
	v_cvt_pk_fp8_f32 v149, v165, v166 op_sel:[0,0,1]
	v_mul_f32_e32 v131, 0x42800000, v40
	v_med3_f32 v131, v131, s62, v236
	s_cmp_lg_u32 s57, 0
	ds_write2_b64 v164, v[132:133], v[148:149] offset1:8
	v_mul_f32_e32 v132, 0x42800000, v44
	v_med3_f32 v149, v132, s62, v236
	v_mov_b32_e32 v132, v130
	v_cvt_pk_fp8_f32 v132, v131, v149
	v_mul_f32_e32 v133, 0x42800000, v36
	v_mul_f32_e32 v148, 0x42800000, v48
	v_med3_f32 v133, v133, s62, v236
	v_med3_f32 v148, v148, s62, v236
	v_cvt_pk_fp8_f32 v132, v133, v148 op_sel:[0,0,1]
	v_mul_f32_e32 v131, 0x42800000, v52
	v_mul_f32_e32 v133, 0x42800000, v56
	v_med3_f32 v131, v131, s62, v236
	v_med3_f32 v165, v133, s62, v236
	v_mov_b32_e32 v133, v130
	v_cvt_pk_fp8_f32 v133, v131, v165
	v_mul_f32_e32 v148, 0x42800000, v64
	v_mul_f32_e32 v149, 0x42800000, v60
	v_med3_f32 v148, v148, s62, v236
	v_med3_f32 v149, v149, s62, v236
	v_cvt_pk_fp8_f32 v133, v148, v149 op_sel:[0,0,1]
	v_mul_f32_e32 v131, 0x42800000, v41
	v_mul_f32_e32 v148, 0x42800000, v45
	v_med3_f32 v131, v131, s62, v236
	v_med3_f32 v166, v148, s62, v236
	v_mov_b32_e32 v148, v130
	v_cvt_pk_fp8_f32 v148, v131, v166
	v_mul_f32_e32 v149, 0x42800000, v37
	v_mul_f32_e32 v165, 0x42800000, v49
	v_med3_f32 v149, v149, s62, v236
	v_med3_f32 v165, v165, s62, v236
	v_cvt_pk_fp8_f32 v148, v149, v165 op_sel:[0,0,1]
	v_mul_f32_e32 v131, 0x42800000, v53
	v_mul_f32_e32 v149, 0x42800000, v57
	v_med3_f32 v131, v131, s62, v236
	v_med3_f32 v167, v149, s62, v236
	v_mov_b32_e32 v149, v130
	v_cvt_pk_fp8_f32 v149, v131, v167
	v_mul_f32_e32 v165, 0x42800000, v65
	v_mul_f32_e32 v166, 0x42800000, v61
	v_med3_f32 v165, v165, s62, v236
	v_med3_f32 v166, v166, s62, v236
	v_cvt_pk_fp8_f32 v149, v165, v166 op_sel:[0,0,1]
	v_add_u32_e32 v131, s56, v156
	ds_write2_b64 v164, v[132:133], v[148:149] offset0:16 offset1:24
	s_cbranch_scc0 .LBB0_870
	s_lshl_b32 s6, s57, 7
	v_lshlrev_b32_e32 v148, 1, v131
	s_waitcnt lgkmcnt(0)
	s_barrier
	s_add_i32 s24, s6, 0xffffff00
	v_and_b32_e32 v133, 0x7f, v131
	v_and_b32_e32 v148, 0xffffff00, v148
	s_and_b32 s7, s58, 0x7f
	v_add_u32_e32 v148, s24, v148
	v_or_b32_e32 v133, s6, v133
	s_lshr_b32 s13, s58, 7
	v_add_u32_e32 v132, s7, v158
	v_cmp_lt_i32_e32 vcc, -1, v148
	v_lshlrev_b32_e32 v133, 7, v133
	s_and_saveexec_b64 s[6:7], vcc
	s_cbranch_execz .LBB0_867
	v_add_u32_e32 v149, v157, v159
	ds_read_b128 v[166:169], v149
	v_lshrrev_b32_e32 v148, 8, v148
	v_mul_u32_u24_e32 v148, s12, v148
	v_add_lshl_u32 v148, v148, s13, 15
	v_and_b32_e32 v149, 0x7f80, v133
	v_add3_u32 v148, v149, v132, v148
	s_waitcnt lgkmcnt(0)
	global_store_dwordx4 v148, v[166:169], s[86:87]

; #define GAS __attribute__((address_space(1)))
; #define LAS __attribute__((address_space(3)))
; #define LDS_BARRIER() do { asm volatile("s_waitcnt lgkmcnt(0)" ::: "memory"); __builtin_amdgcn_s_barrier(); asm volatile("" ::: "memory"); } while (0)
; template <class RowMap>
; __device__ __forceinline__ void conv_store_fp8(const f32x4 (&r)[8], unsigned char* WT, int Kbytes, int k0bytes, int n0, const RowMap rm, LAS unsigned char* T, int tid, int wave, int lane) {
;     const int s = 2 * (lane & 3);
; #pragma unroll
;     for (int j = 0; j < 4; ++j) { const unsigned lo = pk4_fp8(r[0][j] * W8_SCALE, r[1][j] * W8_SCALE, r[2][j] * W8_SCALE, r[3][j] * W8_SCALE), hi = pk4_fp8(r[4][j] * W8_SCALE, r[5][j] * W8_SCALE, r[6][j] * W8_SCALE, r[7][j] * W8_SCALE);
;         *(LAS unsigned long long*)(T + (4 * lane + j) * 64 + 8 * (wave ^ s)) = (unsigned long long)lo | ((unsigned long long)hi << 32); }
;     LDS_BARRIER();
;     const int c16 = tid & 3, rr = tid >> 2;
; #pragma unroll
;     for (int q = 0; q < 2; ++q) { const int row = rr + 128 * q; const v4u v = *(const LAS v4u*)(T + row * 64 + 16 * (c16 ^ ((row >> 2) & 3)));
;         const int dr = rm(n0 + row); if (dr >= 0) *(GAS v4u*)(WT + (unsigned)((((dr >> 8) * (Kbytes >> 7) + (k0bytes >> 7)) << 15) + ((dr & 255) << 7) + (k0bytes & 127) + 16 * c16)) = v; }
;     LDS_BARRIER();
; }
.Lhw_done_4:
	v_mul_f32_e32 v131, 0x42800000, v70
	v_mul_f32_e32 v132, 0x42800000, v74
	v_med3_f32 v131, v131, s62, v236
	v_med3_f32 v149, v132, s62, v236
	v_mov_b32_e32 v132, v130
	v_cvt_pk_fp8_f32 v132, v131, v149
	v_mul_f32_e32 v133, 0x42800000, v66
	v_mul_f32_e32 v148, 0x42800000, v78
	v_med3_f32 v133, v133, s62, v236
	v_med3_f32 v148, v148, s62, v236
	v_cvt_pk_fp8_f32 v132, v133, v148 op_sel:[0,0,1]
	v_mul_f32_e32 v131, 0x42800000, v82
	v_mul_f32_e32 v133, 0x42800000, v86
	v_med3_f32 v131, v131, s62, v236
	v_med3_f32 v165, v133, s62, v236
	v_mov_b32_e32 v133, v130
	v_cvt_pk_fp8_f32 v133, v131, v165
	v_mul_f32_e32 v148, 0x42800000, v94
	v_mul_f32_e32 v149, 0x42800000, v90
	v_med3_f32 v148, v148, s62, v236
	v_med3_f32 v149, v149, s62, v236
	v_cvt_pk_fp8_f32 v133, v148, v149 op_sel:[0,0,1]
	v_mul_f32_e32 v131, 0x42800000, v71
	v_mul_f32_e32 v148, 0x42800000, v75
	v_med3_f32 v131, v131, s62, v236
	v_med3_f32 v166, v148, s62, v236
	v_mov_b32_e32 v148, v130
	v_cvt_pk_fp8_f32 v148, v131, v166
	v_mul_f32_e32 v149, 0x42800000, v67
	v_mul_f32_e32 v165, 0x42800000, v79
	v_med3_f32 v149, v149, s62, v236
	v_med3_f32 v165, v165, s62, v236
	v_cvt_pk_fp8_f32 v148, v149, v165 op_sel:[0,0,1]
	v_mul_f32_e32 v131, 0x42800000, v83
	v_mul_f32_e32 v149, 0x42800000, v87
	v_med3_f32 v131, v131, s62, v236
	v_med3_f32 v167, v149, s62, v236
	v_mov_b32_e32 v149, v130
	v_cvt_pk_fp8_f32 v149, v131, v167
	v_mul_f32_e32 v165, 0x42800000, v95
	v_mul_f32_e32 v166, 0x42800000, v91
	v_med3_f32 v165, v165, s62, v236
	v_med3_f32 v166, v166, s62, v236
	v_cvt_pk_fp8_f32 v149, v165, v166 op_sel:[0,0,1]
	v_mul_f32_e32 v131, 0x42800000, v72
	v_med3_f32 v131, v131, s62, v236
	s_cmp_lg_u32 s27, 0
	ds_write2_b64 v164, v[132:133], v[148:149] offset1:8
	v_mul_f32_e32 v132, 0x42800000, v76
	v_med3_f32 v149, v132, s62, v236
	v_mov_b32_e32 v132, v130
	v_cvt_pk_fp8_f32 v132, v131, v149
	v_mul_f32_e32 v133, 0x42800000, v68
	v_mul_f32_e32 v148, 0x42800000, v80
	v_med3_f32 v133, v133, s62, v236
	v_med3_f32 v148, v148, s62, v236
	v_cvt_pk_fp8_f32 v132, v133, v148 op_sel:[0,0,1]
	v_mul_f32_e32 v131, 0x42800000, v84
	v_mul_f32_e32 v133, 0x42800000, v88
	v_med3_f32 v131, v131, s62, v236
	v_med3_f32 v165, v133, s62, v236
	v_mov_b32_e32 v133, v130
	v_cvt_pk_fp8_f32 v133, v131, v165
	v_mul_f32_e32 v148, 0x42800000, v96
	v_mul_f32_e32 v149, 0x42800000, v92
	v_med3_f32 v148, v148, s62, v236
	v_med3_f32 v149, v149, s62, v236
	v_cvt_pk_fp8_f32 v133, v148, v149 op_sel:[0,0,1]
	v_mul_f32_e32 v131, 0x42800000, v73
	v_mul_f32_e32 v148, 0x42800000, v77
	v_med3_f32 v131, v131, s62, v236
	v_med3_f32 v166, v148, s62, v236
	v_mov_b32_e32 v148, v130
	v_cvt_pk_fp8_f32 v148, v131, v166
	v_mul_f32_e32 v149, 0x42800000, v69
	v_mul_f32_e32 v165, 0x42800000, v81
	v_med3_f32 v149, v149, s62, v236
	v_med3_f32 v165, v165, s62, v236
	v_cvt_pk_fp8_f32 v148, v149, v165 op_sel:[0,0,1]
	v_mul_f32_e32 v131, 0x42800000, v85
	v_mul_f32_e32 v149, 0x42800000, v89
	v_med3_f32 v131, v131, s62, v236
	v_med3_f32 v167, v149, s62, v236
	v_mov_b32_e32 v149, v130
	v_cvt_pk_fp8_f32 v149, v131, v167
	v_mul_f32_e32 v165, 0x42800000, v97
	v_mul_f32_e32 v166, 0x42800000, v93
	v_med3_f32 v165, v165, s62, v236
	v_med3_f32 v166, v166, s62, v236
	v_cvt_pk_fp8_f32 v149, v165, v166 op_sel:[0,0,1]
	v_add_u32_e32 v131, s20, v156
	ds_write2_b64 v164, v[132:133], v[148:149] offset0:16 offset1:24
	s_cbranch_scc0 .LBB0_905
	s_lshl_b32 s6, s27, 7
	v_lshlrev_b32_e32 v148, 1, v131
	s_waitcnt lgkmcnt(0)
	s_barrier
	s_add_i32 s24, s6, 0xffffff00
	v_and_b32_e32 v133, 0x7f, v131
	v_and_b32_e32 v148, 0xffffff00, v148
	s_and_b32 s7, s29, 0x7f
	v_add_u32_e32 v148, s24, v148
	v_or_b32_e32 v133, s6, v133
	s_lshr_b32 s13, s29, 7
	v_add_u32_e32 v132, s7, v158
	v_cmp_lt_i32_e32 vcc, -1, v148
	v_lshlrev_b32_e32 v133, 7, v133
	s_and_saveexec_b64 s[6:7], vcc
	s_cbranch_execz .LBB0_902
	v_add_u32_e32 v149, v157, v159
	ds_read_b128 v[166:169], v149
	v_lshrrev_b32_e32 v148, 8, v148
	v_mul_u32_u24_e32 v148, s12, v148
	v_add_lshl_u32 v148, v148, s13, 15
	v_and_b32_e32 v149, 0x7f80, v133
	v_add3_u32 v148, v149, v132, v148
	s_waitcnt lgkmcnt(0)
	global_store_dwordx4 v148, v[166:169], s[90:91]

; #define GAS __attribute__((address_space(1)))
; #define LAS __attribute__((address_space(3)))
; #define LDS_BARRIER() do { asm volatile("s_waitcnt lgkmcnt(0)" ::: "memory"); __builtin_amdgcn_s_barrier(); asm volatile("" ::: "memory"); } while (0)
; template <class RowMap>
; __device__ __forceinline__ void conv_store_fp8(const f32x4 (&r)[8], unsigned char* WT, int Kbytes, int k0bytes, int n0, const RowMap rm, LAS unsigned char* T, int tid, int wave, int lane) {
;     const int s = 2 * (lane & 3);
; #pragma unroll
;     for (int j = 0; j < 4; ++j) { const unsigned lo = pk4_fp8(r[0][j] * W8_SCALE, r[1][j] * W8_SCALE, r[2][j] * W8_SCALE, r[3][j] * W8_SCALE), hi = pk4_fp8(r[4][j] * W8_SCALE, r[5][j] * W8_SCALE, r[6][j] * W8_SCALE, r[7][j] * W8_SCALE);
;         *(LAS unsigned long long*)(T + (4 * lane + j) * 64 + 8 * (wave ^ s)) = (unsigned long long)lo | ((unsigned long long)hi << 32); }
;     LDS_BARRIER();
;     const int c16 = tid & 3, rr = tid >> 2;
; #pragma unroll
;     for (int q = 0; q < 2; ++q) { const int row = rr + 128 * q; const v4u v = *(const LAS v4u*)(T + row * 64 + 16 * (c16 ^ ((row >> 2) & 3)));
;         const int dr = rm(n0 + row); if (dr >= 0) *(GAS v4u*)(WT + (unsigned)((((dr >> 8) * (Kbytes >> 7) + (k0bytes >> 7)) << 15) + ((dr & 255) << 7) + (k0bytes & 127) + 16 * c16)) = v; }
;     LDS_BARRIER();
; }
.Lhw_done_5:
	v_mul_f32_e32 v131, 0x42800000, v102
	v_mul_f32_e32 v132, 0x42800000, v106
	v_med3_f32 v131, v131, s62, v236
	v_med3_f32 v149, v132, s62, v236
	v_mov_b32_e32 v132, v130
	v_cvt_pk_fp8_f32 v132, v131, v149
	v_mul_f32_e32 v133, 0x42800000, v98
	v_mul_f32_e32 v148, 0x42800000, v110
	v_med3_f32 v133, v133, s62, v236
	v_med3_f32 v148, v148, s62, v236
	v_cvt_pk_fp8_f32 v132, v133, v148 op_sel:[0,0,1]
	v_mul_f32_e32 v131, 0x42800000, v114
	v_mul_f32_e32 v133, 0x42800000, v118
	v_med3_f32 v131, v131, s62, v236
	v_med3_f32 v165, v133, s62, v236
	v_mov_b32_e32 v133, v130
	v_cvt_pk_fp8_f32 v133, v131, v165
	v_mul_f32_e32 v148, 0x42800000, v126
	v_mul_f32_e32 v149, 0x42800000, v122
	v_med3_f32 v148, v148, s62, v236
	v_med3_f32 v149, v149, s62, v236
	v_cvt_pk_fp8_f32 v133, v148, v149 op_sel:[0,0,1]
	v_mul_f32_e32 v131, 0x42800000, v103
	v_mul_f32_e32 v148, 0x42800000, v107
	v_med3_f32 v131, v131, s62, v236
	v_med3_f32 v166, v148, s62, v236
	v_mov_b32_e32 v148, v130
	v_cvt_pk_fp8_f32 v148, v131, v166
	v_mul_f32_e32 v149, 0x42800000, v99
	v_mul_f32_e32 v165, 0x42800000, v111
	v_med3_f32 v149, v149, s62, v236
	v_med3_f32 v165, v165, s62, v236
	v_cvt_pk_fp8_f32 v148, v149, v165 op_sel:[0,0,1]
	v_mul_f32_e32 v131, 0x42800000, v115
	v_mul_f32_e32 v149, 0x42800000, v119
	v_med3_f32 v131, v131, s62, v236
	v_med3_f32 v167, v149, s62, v236
	v_mov_b32_e32 v149, v130
	v_cvt_pk_fp8_f32 v149, v131, v167
	v_mul_f32_e32 v165, 0x42800000, v127
	v_mul_f32_e32 v166, 0x42800000, v123
	v_med3_f32 v165, v165, s62, v236
	v_med3_f32 v166, v166, s62, v236
	v_cvt_pk_fp8_f32 v149, v165, v166 op_sel:[0,0,1]
	v_mul_f32_e32 v131, 0x42800000, v104
	v_med3_f32 v131, v131, s62, v236
	s_cmp_lg_u32 s24, 0
	ds_write2_b64 v164, v[132:133], v[148:149] offset1:8
	v_mul_f32_e32 v132, 0x42800000, v108
	v_med3_f32 v149, v132, s62, v236
	v_mov_b32_e32 v132, v130
	v_cvt_pk_fp8_f32 v132, v131, v149
	v_mul_f32_e32 v133, 0x42800000, v100
	v_mul_f32_e32 v148, 0x42800000, v112
	v_med3_f32 v133, v133, s62, v236
	v_med3_f32 v148, v148, s62, v236
	v_cvt_pk_fp8_f32 v132, v133, v148 op_sel:[0,0,1]
	v_mul_f32_e32 v131, 0x42800000, v116
	v_mul_f32_e32 v133, 0x42800000, v120
	v_med3_f32 v131, v131, s62, v236
	v_med3_f32 v165, v133, s62, v236
	v_mov_b32_e32 v133, v130
	v_cvt_pk_fp8_f32 v133, v131, v165
	v_mul_f32_e32 v148, 0x42800000, v128
	v_mul_f32_e32 v149, 0x42800000, v124
	v_med3_f32 v148, v148, s62, v236
	v_med3_f32 v149, v149, s62, v236
	v_cvt_pk_fp8_f32 v133, v148, v149 op_sel:[0,0,1]
	v_mul_f32_e32 v131, 0x42800000, v105
	v_mul_f32_e32 v148, 0x42800000, v109
	v_med3_f32 v131, v131, s62, v236
	v_med3_f32 v166, v148, s62, v236
	v_mov_b32_e32 v148, v130
	v_cvt_pk_fp8_f32 v148, v131, v166
	v_mul_f32_e32 v149, 0x42800000, v101
	v_mul_f32_e32 v165, 0x42800000, v113
	v_med3_f32 v149, v149, s62, v236
	v_med3_f32 v165, v165, s62, v236
	v_cvt_pk_fp8_f32 v148, v149, v165 op_sel:[0,0,1]
	v_mul_f32_e32 v131, 0x42800000, v117
	v_mul_f32_e32 v149, 0x42800000, v121
	v_med3_f32 v131, v131, s62, v236
	v_med3_f32 v167, v149, s62, v236
	v_mov_b32_e32 v149, v130
	v_cvt_pk_fp8_f32 v149, v131, v167
	v_mul_f32_e32 v165, 0x42800000, v129
	v_mul_f32_e32 v166, 0x42800000, v125
	v_med3_f32 v165, v165, s62, v236
	v_med3_f32 v166, v166, s62, v236
	v_cvt_pk_fp8_f32 v149, v165, v166 op_sel:[0,0,1]
	v_add_u32_e32 v131, s19, v156
	ds_write2_b64 v164, v[132:133], v[148:149] offset0:16 offset1:24
	s_cbranch_scc0 .LBB0_941
	s_waitcnt lgkmcnt(0)
	s_lshl_b32 s4, s24, 7
	v_lshlrev_b32_e32 v148, 1, v131
	s_waitcnt lgkmcnt(0)
	s_barrier
	s_add_i32 s7, s4, 0xffffff00
	v_and_b32_e32 v133, 0x7f, v131
	v_and_b32_e32 v148, 0xffffff00, v148
	s_and_b32 s5, s18, 0x7f
	v_add_u32_e32 v148, s7, v148
	v_or_b32_e32 v133, s4, v133
	s_lshr_b32 s6, s18, 7
	v_add_u32_e32 v132, s5, v158
	v_cmp_lt_i32_e32 vcc, -1, v148
	v_lshlrev_b32_e32 v133, 7, v133
	s_and_saveexec_b64 s[4:5], vcc
	s_cbranch_execz .LBB0_938
	v_add_u32_e32 v149, v157, v159
	ds_read_b128 v[166:169], v149
	v_lshrrev_b32_e32 v148, 8, v148
	v_mul_u32_u24_e32 v148, s2, v148
	v_add_lshl_u32 v148, v148, s6, 15
	v_and_b32_e32 v149, 0x7f80, v133
	v_add3_u32 v148, v149, v132, v148
	s_waitcnt lgkmcnt(0)
	global_store_dwordx4 v148, v[166:169], s[50:51]

; #define CV_LOAD(j, R) do { ConvTile c_; if (CV_VALID(j) && CV_DEC(CV_TILE(j), c_)) conv_load(c_.W, c_.N, c_.k0, c_.n0, wave, lane, R); } while (0)
; #define CV_PROC(j, R) { ConvTile c_; if (!CV_VALID(j) || !CV_DEC(CV_TILE(j), c_)) break; if constexpr (MOE) conv_emit_moe(c_, R, T, tid, wave, lane); else conv_emit(c_, R, T, tid, wave, lane); }
; template <int NSLOT, bool MOE> __device__ __forceinline__ void conv_burst(const ConvHook& h, int bid, PG8_LAS unsigned char* T_, int tid) {
;     ...
;     const int p0 = (h.t0 >> 1) + bid, p1 = h.t1 >> 1;
;     ...
;     if constexpr (NSLOT == 4) {
;         f32x4 R0[8], R1[8], R2[8], R3[8];
;         CV_LOAD(0, R0); CV_LOAD(1, R1); CV_LOAD(2, R2);
;         for (int j = 0;; j += 4) {
;             CV_LOAD(j + 3, R3); CV_PROC(j, R0)
.LBB0_2316:
	s_and_b32 s2, s19, 0x7ffffe00
	s_add_i32 s2, s74, s2
	s_addk_i32 s2, 0x100
	s_add_i32 s100, s2, 0x200
	s_cmpk_lt_i32 s100, 0x2646
	s_cselect_b32 s100, 1, 0
	s_cmpk_lt_i32 s2, 0x2646
	s_cselect_b64 s[4:5], -1, 0
	s_cmpk_gt_i32 s2, 0x2645
	s_cbranch_scc1 .LBB0_2330
	s_lshl_b32 s18, s2, 1
	s_or_b32 s33, s18, 1
	s_cmpk_gt_i32 s33, 0x47ff
	s_mov_b64 s[12:13], -1
	s_cbranch_scc0 .LBB0_2319
	s_add_i32 s33, s33, 0xb800
	s_bfe_u32 s6, s33, 0x90007
	s_mulk_i32 s6, 0x2493
	s_lshr_b32 s12, s6, 16
	s_load_dwordx2 s[6:7], s[14:15], 0xe0
	s_mul_i32 s13, s12, 0x380
	s_sub_i32 s13, s33, s13
	s_and_b32 s13, s13, 0xffff
	s_mul_hi_u32 s24, s12, 0x3800000
	s_mul_i32 s12, s12, 0x3800000
	s_waitcnt lgkmcnt(0)
	s_add_u32 s6, s6, s12
	s_addc_u32 s7, s7, s24
	s_lshl_b32 s12, s13, 3
	s_lshl_b32 s24, s13, 6
	s_and_b32 s12, s12, 0x1f80
	s_and_b32 s24, s24, 64
	s_or_b32 s24, s12, s24
	s_lshl_b32 s12, s13, 7
	s_and_b32 s26, s12, 0x700
	s_mov_b64 s[12:13], 0

; #define GAS __attribute__((address_space(1)))
; #define CV_LOAD(j, R) do { ConvTile c_; if (CV_VALID(j) && CV_DEC(CV_TILE(j), c_)) conv_load(c_.W, c_.N, c_.k0, c_.n0, wave, lane, R); } while (0)
; __device__ __forceinline__ void conv_load(const float* W, int N, int k0, int n0, int wave, int lane, f32x4 (&r)[8]) {
;     const int n = n0 + 4 * lane; const bool ok = n < N;
;     const float* p = W + (size_t)(k0 + 8 * wave) * N + n;
; #pragma unroll
;     for (int i = 0; i < 8; ++i) r[i] = ok ? __builtin_nontemporal_load((const GAS f32x4*)(p + (size_t)i * N)) : (f32x4){0.f, 0.f, 0.f, 0.f};
; template <int NSLOT, bool MOE> __device__ __forceinline__ void conv_burst(const ConvHook& h, int bid, PG8_LAS unsigned char* T_, int tid) {
;     ...
;     if constexpr (NSLOT == 4) {
;         f32x4 R0[8], R1[8], R2[8], R3[8];
;         CV_LOAD(0, R0); CV_LOAD(1, R1); CV_LOAD(2, R2);
.LBB0_2321:
	s_add_i32 s13, s24, s31
	s_waitcnt lgkmcnt(0)
	s_mul_hi_i32 s55, s13, s12
	s_mul_i32 s54, s13, s12
	s_lshl_b64 s[54:55], s[54:55], 2
	s_cmp_lg_u32 s100, 0
	s_cbranch_scc1 .Lhw_fast_6
	s_waitcnt vmcnt(0)
	s_branch .Lhw_done_6
.Lhw_fast_6:
.Lhw_done_6:
	v_or_b32_e32 v90, s26, v157
	s_add_u32 s6, s6, s54
	s_addc_u32 s7, s7, s55
	v_ashrrev_i32_e32 v91, 31, v90
	v_cmp_gt_i32_e32 vcc, s12, v90
	v_lshl_add_u64 v[132:133], v[90:91], 2, s[6:7]
	v_mov_b32_e32 v90, 0
	v_mov_b32_e32 v94, 0
	v_mov_b32_e32 v95, 0
	v_mov_b32_e32 v96, 0
	v_mov_b32_e32 v97, 0
	v_mov_b32_e32 v98, 0
	v_mov_b32_e32 v99, 0
	v_mov_b32_e32 v100, 0
	v_mov_b32_e32 v101, 0
	s_and_saveexec_b64 s[6:7], vcc
	s_cbranch_execz .LBB0_2323
	s_lshl_b32 s24, s12, 2
	v_lshl_add_u64 v[92:93], v[132:133], 0, s[24:25]
	global_load_dwordx4 v[94:97], v[132:133], off nt
	global_load_dwordx4 v[98:101], v[92:93], off nt

; #define LAS __attribute__((address_space(3)))
; #define LDS_BARRIER() do { asm volatile("s_waitcnt lgkmcnt(0)" ::: "memory"); __builtin_amdgcn_s_barrier(); asm volatile("" ::: "memory"); } while (0)
; template <class RowMap>
; __device__ __forceinline__ void conv_store_fp8(const f32x4 (&r)[8], unsigned char* WT, int Kbytes, int k0bytes, int n0, const RowMap rm, LAS unsigned char* T, int tid, int wave, int lane) {
;     const int s = 2 * (lane & 3);
; #pragma unroll
;     for (int j = 0; j < 4; ++j) { const unsigned lo = pk4_fp8(r[0][j] * W8_SCALE, r[1][j] * W8_SCALE, r[2][j] * W8_SCALE, r[3][j] * W8_SCALE), hi = pk4_fp8(r[4][j] * W8_SCALE, r[5][j] * W8_SCALE, r[6][j] * W8_SCALE, r[7][j] * W8_SCALE);
;         *(LAS unsigned long long*)(T + (4 * lane + j) * 64 + 8 * (wave ^ s)) = (unsigned long long)lo | ((unsigned long long)hi << 32); }
;     LDS_BARRIER();
.LBB0_2336:
	s_cmp_lg_u32 s100, 0
	s_cbranch_scc1 .Lhw_fast_7
	s_waitcnt vmcnt(0)
	s_branch .Lhw_done_7

; #define GAS __attribute__((address_space(1)))
; #define LAS __attribute__((address_space(3)))
; #define LDS_BARRIER() do { asm volatile("s_waitcnt lgkmcnt(0)" ::: "memory"); __builtin_amdgcn_s_barrier(); asm volatile("" ::: "memory"); } while (0)
; template <class RowMap>
; __device__ __forceinline__ void conv_store_fp8(const f32x4 (&r)[8], unsigned char* WT, int Kbytes, int k0bytes, int n0, const RowMap rm, LAS unsigned char* T, int tid, int wave, int lane) {
;     const int s = 2 * (lane & 3);
; #pragma unroll
;     for (int j = 0; j < 4; ++j) { const unsigned lo = pk4_fp8(r[0][j] * W8_SCALE, r[1][j] * W8_SCALE, r[2][j] * W8_SCALE, r[3][j] * W8_SCALE), hi = pk4_fp8(r[4][j] * W8_SCALE, r[5][j] * W8_SCALE, r[6][j] * W8_SCALE, r[7][j] * W8_SCALE);
;         *(LAS unsigned long long*)(T + (4 * lane + j) * 64 + 8 * (wave ^ s)) = (unsigned long long)lo | ((unsigned long long)hi << 32); }
;     LDS_BARRIER();
;     const int c16 = tid & 3, rr = tid >> 2;
; #pragma unroll
;     for (int q = 0; q < 2; ++q) { const int row = rr + 128 * q; const v4u v = *(const LAS v4u*)(T + row * 64 + 16 * (c16 ^ ((row >> 2) & 3)));
;         const int dr = rm(n0 + row); if (dr >= 0) *(GAS v4u*)(WT + (unsigned)((((dr >> 8) * (Kbytes >> 7) + (k0bytes >> 7)) << 15) + ((dr & 255) << 7) + (k0bytes & 127) + 16 * c16)) = v; }
;     LDS_BARRIER();
; }
.Lhw_done_7:
	v_mul_f32_e32 v131, 0x42800000, v2
	v_mul_f32_e32 v132, 0x42800000, v6
	v_med3_f32 v131, v131, s62, v236
	v_med3_f32 v153, v132, s62, v236
	v_mov_b32_e32 v132, v130
	v_cvt_pk_fp8_f32 v132, v131, v153
	v_mul_f32_e32 v133, 0x42800000, v10
	v_mul_f32_e32 v152, 0x42800000, v14
	v_med3_f32 v133, v133, s62, v236
	v_med3_f32 v152, v152, s62, v236
	v_cvt_pk_fp8_f32 v132, v133, v152 op_sel:[0,0,1]
	v_mul_f32_e32 v131, 0x42800000, v18
	v_mul_f32_e32 v133, 0x42800000, v22
	v_med3_f32 v131, v131, s62, v236
	v_med3_f32 v158, v133, s62, v236
	v_mov_b32_e32 v133, v130
	v_cvt_pk_fp8_f32 v133, v131, v158
	v_mul_f32_e32 v152, 0x42800000, v50
	v_mul_f32_e32 v153, 0x42800000, v54
	v_med3_f32 v152, v152, s62, v236
	v_med3_f32 v153, v153, s62, v236
	v_cvt_pk_fp8_f32 v133, v152, v153 op_sel:[0,0,1]
	v_mul_f32_e32 v131, 0x42800000, v3
	v_mul_f32_e32 v152, 0x42800000, v7
	v_med3_f32 v131, v131, s62, v236
	v_med3_f32 v159, v152, s62, v236
	v_mov_b32_e32 v152, v130
	v_cvt_pk_fp8_f32 v152, v131, v159
	v_mul_f32_e32 v153, 0x42800000, v11
	v_mul_f32_e32 v158, 0x42800000, v15
	v_med3_f32 v153, v153, s62, v236
	v_med3_f32 v158, v158, s62, v236
	v_cvt_pk_fp8_f32 v152, v153, v158 op_sel:[0,0,1]
	v_mul_f32_e32 v131, 0x42800000, v19
	v_mul_f32_e32 v153, 0x42800000, v23
	v_med3_f32 v131, v131, s62, v236
	v_med3_f32 v172, v153, s62, v236
	v_mov_b32_e32 v153, v130
	v_cvt_pk_fp8_f32 v153, v131, v172
	v_mul_f32_e32 v158, 0x42800000, v51
	v_mul_f32_e32 v159, 0x42800000, v55
	v_med3_f32 v158, v158, s62, v236
	v_med3_f32 v159, v159, s62, v236
	v_cvt_pk_fp8_f32 v153, v158, v159 op_sel:[0,0,1]
	v_mul_f32_e32 v131, 0x42800000, v4
	v_med3_f32 v131, v131, s62, v236
	s_cmp_lg_u32 s12, 0
	ds_write2_b64 v171, v[132:133], v[152:153] offset1:8
	v_mul_f32_e32 v132, 0x42800000, v8
	v_med3_f32 v153, v132, s62, v236
	v_mov_b32_e32 v132, v130
	v_cvt_pk_fp8_f32 v132, v131, v153
	v_mul_f32_e32 v133, 0x42800000, v12
	v_mul_f32_e32 v152, 0x42800000, v16
	v_med3_f32 v133, v133, s62, v236
	v_med3_f32 v152, v152, s62, v236
	v_cvt_pk_fp8_f32 v132, v133, v152 op_sel:[0,0,1]
	v_mul_f32_e32 v131, 0x42800000, v20
	v_mul_f32_e32 v133, 0x42800000, v24
	v_med3_f32 v131, v131, s62, v236
	v_med3_f32 v158, v133, s62, v236
	v_mov_b32_e32 v133, v130
	v_cvt_pk_fp8_f32 v133, v131, v158
	v_mul_f32_e32 v152, 0x42800000, v52
	v_mul_f32_e32 v153, 0x42800000, v56
	v_med3_f32 v152, v152, s62, v236
	v_med3_f32 v153, v153, s62, v236
	v_cvt_pk_fp8_f32 v133, v152, v153 op_sel:[0,0,1]
	v_mul_f32_e32 v131, 0x42800000, v5
	v_mul_f32_e32 v152, 0x42800000, v9
	v_med3_f32 v131, v131, s62, v236
	v_med3_f32 v159, v152, s62, v236
	v_mov_b32_e32 v152, v130
	v_cvt_pk_fp8_f32 v152, v131, v159
	v_mul_f32_e32 v153, 0x42800000, v13
	v_mul_f32_e32 v158, 0x42800000, v17
	v_med3_f32 v153, v153, s62, v236
	v_med3_f32 v158, v158, s62, v236
	v_cvt_pk_fp8_f32 v152, v153, v158 op_sel:[0,0,1]
	v_mul_f32_e32 v131, 0x42800000, v21
	v_mul_f32_e32 v153, 0x42800000, v25
	v_med3_f32 v131, v131, s62, v236
	v_med3_f32 v172, v153, s62, v236
	v_mov_b32_e32 v153, v130
	v_cvt_pk_fp8_f32 v153, v131, v172
	v_mul_f32_e32 v158, 0x42800000, v53
	v_mul_f32_e32 v159, 0x42800000, v57
	v_med3_f32 v158, v158, s62, v236
	v_med3_f32 v159, v159, s62, v236
	v_cvt_pk_fp8_f32 v153, v158, v159 op_sel:[0,0,1]
	ds_write2_b64 v171, v[132:133], v[152:153] offset0:16 offset1:24
	s_cbranch_scc0 .LBB0_2350
	s_lshl_b32 s12, s12, 7
	v_add_lshl_u32 v132, s24, v160, 1
	s_waitcnt lgkmcnt(0)
	s_barrier
	s_add_i32 s47, s12, 0xffffff00
	v_and_b32_e32 v132, 0xffffff00, v132
	s_and_b32 s13, s33, 0x7f
	v_add_u32_e32 v133, s47, v132
	v_or_b32_e32 v132, s12, v166
	s_lshr_b32 s37, s33, 7
	v_add_u32_e32 v131, s13, v162
	v_cmp_lt_i32_e32 vcc, -1, v133
	v_lshlrev_b32_e32 v132, 7, v132
	s_and_saveexec_b64 s[12:13], vcc
	s_cbranch_execz .LBB0_2339
	v_add_u32_e32 v152, v161, v163
	ds_read_b128 v[172:175], v152
	v_lshrrev_b32_e32 v133, 8, v133
	v_mul_u32_u24_e32 v133, s26, v133
	v_add_lshl_u32 v133, v133, s37, 15
	v_and_b32_e32 v152, 0x7f80, v132
	v_add3_u32 v133, v152, v131, v133
	s_waitcnt lgkmcnt(0)
	global_store_dwordx4 v133, v[172:175], s[6:7]

; #define CV_LOAD(j, R) do { ConvTile c_; if (CV_VALID(j) && CV_DEC(CV_TILE(j), c_)) conv_load(c_.W, c_.N, c_.k0, c_.n0, wave, lane, R); } while (0)
; #define CV_PROC(j, R) { ConvTile c_; if (!CV_VALID(j) || !CV_DEC(CV_TILE(j), c_)) break; if constexpr (MOE) conv_emit_moe(c_, R, T, tid, wave, lane); else conv_emit(c_, R, T, tid, wave, lane); }
; template <int NSLOT, bool MOE> __device__ __forceinline__ void conv_burst(const ConvHook& h, int bid, PG8_LAS unsigned char* T_, int tid) {
;     ...
;     if constexpr (NSLOT == 4) {
;         f32x4 R0[8], R1[8], R2[8], R3[8];
;         CV_LOAD(0, R0); CV_LOAD(1, R1); CV_LOAD(2, R2);
;         for (int j = 0;; j += 4) {
;             CV_LOAD(j + 3, R3); CV_PROC(j, R0)
;             CV_LOAD(j + 4, R0); CV_PROC(j + 1, R1)
;             CV_LOAD(j + 5, R1); CV_PROC(j + 2, R2)
.LBB0_2369:
	s_cmp_lg_u32 s100, 0
	s_cbranch_scc1 .Lhw_fast_8
	s_branch .Lhw_done_8
